# phase 9 reuses the expert unit tables that phase 8 left in LDS (same launch, same counts) instead of rebuilding them
# speedup vs baseline: 1.0105x; 1.0008x over previous
.LBB0_1075:
	s_cmp_lt_i32 s78, 10
	s_cselect_b64 s[4:5], -1, 0
	s_and_b64 s[4:5], s[4:5], s[6:7]
	s_andn2_b64 vcc, exec, s[4:5]
	s_cbranch_vccnz .LBB0_1097
	v_mov_b32_e32 v2, v250
	s_nop 0
	v_readfirstlane_b32 s10, v2
	v_cmp_gt_i32_e32 vcc, 64, v2
	s_and_saveexec_b64 s[6:7], vcc
	s_cbranch_execz .LBB0_1078
	s_cmp_lt_i32 s78, 9
	s_cbranch_scc1 .LBB0_1078
	v_ashrrev_i32_e32 v3, 31, v2
	v_lshl_add_u64 v[0:1], v[2:3], 2, s[76:77]
	s_mov_b64 s[8:9], 0x4000
	v_lshl_add_u64 v[4:5], v[0:1], 0, s[8:9]
	v_add_co_u32_e32 v0, vcc, 0x4000, v0
	s_movk_i32 s3, 0x44
	s_nop 0
	v_addc_co_u32_e32 v1, vcc, 0, v1, vcc
	global_load_dword v3, v[0:1], off
	global_load_dword v6, v[4:5], off offset:256
	global_load_dword v7, v[4:5], off offset:512
	global_load_dword v8, v[4:5], off offset:768
	global_load_dword v9, v[4:5], off offset:1024
	global_load_dword v10, v[4:5], off offset:1280
	global_load_dword v11, v[4:5], off offset:1536
	global_load_dword v12, v[4:5], off offset:1792
	global_load_dword v13, v[4:5], off offset:2048
	global_load_dword v14, v[4:5], off offset:2304
	global_load_dword v15, v[4:5], off offset:2560
	global_load_dword v16, v[4:5], off offset:2816
	global_load_dword v17, v[4:5], off offset:3072
	global_load_dword v18, v[4:5], off offset:3328
	global_load_dword v19, v[4:5], off offset:3584
	global_load_dword v0, v[4:5], off offset:3840
	s_add_i32 s8, 0, 0x20000
	v_mul_lo_u32 v4, v2, s3
	v_mov_b32_e32 v1, 0
	v_add_u32_e32 v4, s8, v4
	ds_write_b32 v4, v1 offset:1024
	v_add_u32_e32 v1, 0x404, v4
	s_waitcnt vmcnt(0)
	v_add_u32_e32 v20, 0x40c, v4
	v_add_u32_e32 v21, 0x414, v4
	v_add_u32_e32 v22, 0x41c, v4
	v_add_u32_e32 v23, 0x424, v4
	v_add_u32_e32 v24, 0x42c, v4
	v_add_u32_e32 v25, 0x434, v4
	v_add_u32_e32 v4, 0x43c, v4
	v_lshl_add_u32 v5, v2, 2, s8
	v_add_u32_e32 v6, v6, v3
	ds_write2_b32 v1, v3, v6 offset1:1
	v_add_u32_e32 v1, v7, v6
	v_add_u32_e32 v3, v8, v1
	ds_write2_b32 v20, v1, v3 offset1:1
	v_add_u32_e32 v1, v9, v3
	v_add_u32_e32 v3, v10, v1
	ds_write2_b32 v21, v1, v3 offset1:1
	v_add_u32_e32 v1, v11, v3
	v_add_u32_e32 v3, v12, v1
	ds_write2_b32 v22, v1, v3 offset1:1
	v_add_u32_e32 v1, v13, v3
	v_add_u32_e32 v3, v14, v1
	ds_write2_b32 v23, v1, v3 offset1:1
	v_add_u32_e32 v1, v15, v3
	v_add_u32_e32 v3, v16, v1
	ds_write2_b32 v24, v1, v3 offset1:1
	v_add_u32_e32 v1, v17, v3
	v_add_u32_e32 v3, v18, v1
	ds_write2_b32 v25, v1, v3 offset1:1
	v_add_u32_e32 v1, v19, v3
	v_add_u32_e32 v0, v0, v1
	ds_write2_b32 v4, v1, v0 offset1:1
	ds_write_b32 v5, v0 offset:320
.LBB0_1078:
	s_or_b64 exec, exec, s[6:7]
	v_cmp_eq_u32_e32 vcc, 0, v2
	s_waitcnt vmcnt(0) lgkmcnt(0)
	s_barrier
	s_and_saveexec_b64 s[6:7], vcc
	s_cbranch_execz .LBB0_1080
	s_cmp_lt_i32 s78, 9
	s_cbranch_scc1 .LBB0_1080
	s_add_i32 s3, 0, 0x20140
	v_mov_b32_e32 v0, s3
	ds_read_b128 v[4:7], v0
	s_add_i32 s3, 0, 0x20150
	v_mov_b32_e32 v0, s3
	ds_read_b128 v[8:11], v0
	s_add_i32 s3, 0, 0x20000
	s_waitcnt lgkmcnt(1)
	v_add_u32_e32 v0, 0x1ff, v4
	v_ashrrev_i32_e32 v0, 9, v0
	v_max_i32_e32 v17, 1, v0
	v_add_u32_e32 v0, 0x1ff, v5
	v_ashrrev_i32_e32 v0, 9, v0
	v_max_i32_e32 v0, 1, v0
	v_add_u32_e32 v18, v0, v17
	v_add_u32_e32 v0, 0x1ff, v6
	v_ashrrev_i32_e32 v0, 9, v0
	v_max_i32_e32 v0, 1, v0
	v_add_u32_e32 v14, v5, v4
	v_add_u32_e32 v19, v0, v18
	v_mov_b32_e32 v16, 0
	v_mov_b32_e32 v0, s3
	s_add_i32 s3, 0, 0x20280
	v_add_u32_e32 v15, v6, v14
	ds_write_b128 v0, v[16:19]
	v_mov_b32_e32 v12, v16
	v_mov_b32_e32 v13, v4
	v_mov_b32_e32 v0, s3
	ds_write_b128 v0, v[12:15]
	v_add_u32_e32 v0, 0x1ff, v7
	v_ashrrev_i32_e32 v0, 9, v0
	v_max_i32_e32 v0, 1, v0
	v_add_u32_e32 v12, v0, v19
	s_waitcnt lgkmcnt(2)
	v_add_u32_e32 v0, 0x1ff, v8
	v_ashrrev_i32_e32 v0, 9, v0
	v_max_i32_e32 v0, 1, v0
	v_add_u32_e32 v13, v0, v12
	v_add_u32_e32 v0, 0x1ff, v9
	v_ashrrev_i32_e32 v0, 9, v0
	v_max_i32_e32 v0, 1, v0
	v_add_u32_e32 v14, v0, v13
	v_add_u32_e32 v0, 0x1ff, v10
	v_ashrrev_i32_e32 v0, 9, v0
	v_add_u32_e32 v4, v7, v15
	v_max_i32_e32 v0, 1, v0
	s_add_i32 s3, 0, 0x20010
	v_add_u32_e32 v5, v8, v4
	v_add_u32_e32 v15, v0, v14
	v_mov_b32_e32 v0, s3
	s_add_i32 s3, 0, 0x20290
	v_add_u32_e32 v6, v9, v5
	ds_write_b128 v0, v[12:15]
	v_mov_b32_e32 v0, s3
	s_add_i32 s3, 0, 0x20160
	v_add_u32_e32 v7, v10, v6
	v_mov_b32_e32 v1, s3
	ds_write_b128 v0, v[4:7]
	v_add_u32_e32 v4, v11, v7
	ds_read_b128 v[6:9], v1
	v_add_u32_e32 v0, 0x1ff, v11
	v_ashrrev_i32_e32 v0, 9, v0
	v_max_i32_e32 v0, 1, v0
	s_add_i32 s3, 0, 0x20170
	v_add_u32_e32 v10, v0, v15
	v_mov_b32_e32 v0, s3
	ds_read_b128 v[14:17], v0
	s_waitcnt lgkmcnt(1)
	v_add_u32_e32 v0, 0x1ff, v6
	v_ashrrev_i32_e32 v0, 9, v0
	v_max_i32_e32 v0, 1, v0
	v_add_u32_e32 v11, v0, v10
	v_add_u32_e32 v0, 0x1ff, v7
	v_ashrrev_i32_e32 v0, 9, v0
	v_max_i32_e32 v0, 1, v0
	v_add_u32_e32 v12, v0, v11
	v_add_u32_e32 v0, 0x1ff, v8
	v_ashrrev_i32_e32 v0, 9, v0
	v_add_u32_e32 v5, v6, v4
	v_max_i32_e32 v0, 1, v0
	s_add_i32 s3, 0, 0x20020
	v_add_u32_e32 v6, v7, v5
	v_add_u32_e32 v13, v0, v12
	v_mov_b32_e32 v0, s3
	s_add_i32 s3, 0, 0x202a0
	v_add_u32_e32 v7, v8, v6
	ds_write_b128 v0, v[10:13]
	v_mov_b32_e32 v0, s3
	ds_write_b128 v0, v[4:7]
	v_add_u32_e32 v0, 0x1ff, v9
	v_ashrrev_i32_e32 v0, 9, v0
	v_max_i32_e32 v0, 1, v0
	v_add_u32_e32 v8, v0, v13
	s_waitcnt lgkmcnt(2)
	v_add_u32_e32 v0, 0x1ff, v14
	v_ashrrev_i32_e32 v0, 9, v0
	v_max_i32_e32 v0, 1, v0
	v_add_u32_e32 v4, v9, v7
	v_add_u32_e32 v9, v0, v8
	v_add_u32_e32 v0, 0x1ff, v15
	v_ashrrev_i32_e32 v0, 9, v0
	v_max_i32_e32 v0, 1, v0
	v_add_u32_e32 v10, v0, v9
	v_add_u32_e32 v0, 0x1ff, v16
	v_ashrrev_i32_e32 v0, 9, v0
	v_max_i32_e32 v0, 1, v0
	s_add_i32 s3, 0, 0x20030
	v_add_u32_e32 v5, v14, v4
	v_add_u32_e32 v11, v0, v10
	v_mov_b32_e32 v0, s3
	s_add_i32 s3, 0, 0x202b0
	v_add_u32_e32 v6, v15, v5
	ds_write_b128 v0, v[8:11]
	v_mov_b32_e32 v0, s3
	s_add_i32 s3, 0, 0x20180
	v_add_u32_e32 v7, v16, v6
	v_mov_b32_e32 v1, s3
	ds_write_b128 v0, v[4:7]
	v_add_u32_e32 v4, v17, v7
	ds_read_b128 v[6:9], v1
	v_add_u32_e32 v0, 0x1ff, v17
	v_ashrrev_i32_e32 v0, 9, v0
	v_max_i32_e32 v0, 1, v0
	s_add_i32 s3, 0, 0x20190
	v_add_u32_e32 v10, v0, v11
	v_mov_b32_e32 v0, s3
	ds_read_b128 v[14:17], v0
	s_waitcnt lgkmcnt(1)
	v_add_u32_e32 v0, 0x1ff, v6
	v_ashrrev_i32_e32 v0, 9, v0
	v_max_i32_e32 v0, 1, v0
	v_add_u32_e32 v11, v0, v10
	v_add_u32_e32 v0, 0x1ff, v7
	v_ashrrev_i32_e32 v0, 9, v0
	v_max_i32_e32 v0, 1, v0
	v_add_u32_e32 v12, v0, v11
	v_add_u32_e32 v0, 0x1ff, v8
	v_ashrrev_i32_e32 v0, 9, v0
	v_add_u32_e32 v5, v6, v4
	v_max_i32_e32 v0, 1, v0
	s_add_i32 s3, 0, 0x20040
	v_add_u32_e32 v6, v7, v5
	v_add_u32_e32 v13, v0, v12
	v_mov_b32_e32 v0, s3
	s_add_i32 s3, 0, 0x202c0
	v_add_u32_e32 v7, v8, v6
	ds_write_b128 v0, v[10:13]
	v_mov_b32_e32 v0, s3
	ds_write_b128 v0, v[4:7]
	v_add_u32_e32 v0, 0x1ff, v9
	v_ashrrev_i32_e32 v0, 9, v0
	v_max_i32_e32 v0, 1, v0
	v_add_u32_e32 v8, v0, v13
	s_waitcnt lgkmcnt(2)
	v_add_u32_e32 v0, 0x1ff, v14
	v_ashrrev_i32_e32 v0, 9, v0
	v_max_i32_e32 v0, 1, v0
	v_add_u32_e32 v4, v9, v7
	v_add_u32_e32 v9, v0, v8
	v_add_u32_e32 v0, 0x1ff, v15
	v_ashrrev_i32_e32 v0, 9, v0
	v_max_i32_e32 v0, 1, v0
	v_add_u32_e32 v10, v0, v9
	v_add_u32_e32 v0, 0x1ff, v16
	v_ashrrev_i32_e32 v0, 9, v0
	v_max_i32_e32 v0, 1, v0
	s_add_i32 s3, 0, 0x20050
	v_add_u32_e32 v5, v14, v4
	v_add_u32_e32 v11, v0, v10
	v_mov_b32_e32 v0, s3
	s_add_i32 s3, 0, 0x202d0
	v_add_u32_e32 v6, v15, v5
	ds_write_b128 v0, v[8:11]
	v_mov_b32_e32 v0, s3
	s_add_i32 s3, 0, 0x201a0
	v_add_u32_e32 v7, v16, v6
	v_mov_b32_e32 v1, s3
	ds_write_b128 v0, v[4:7]
	v_add_u32_e32 v4, v17, v7
	ds_read_b128 v[6:9], v1
	v_add_u32_e32 v0, 0x1ff, v17
	v_ashrrev_i32_e32 v0, 9, v0
	v_max_i32_e32 v0, 1, v0
	s_add_i32 s3, 0, 0x201b0
	v_add_u32_e32 v10, v0, v11
	v_mov_b32_e32 v0, s3
	ds_read_b128 v[14:17], v0
	s_waitcnt lgkmcnt(1)
	v_add_u32_e32 v0, 0x1ff, v6
	v_ashrrev_i32_e32 v0, 9, v0
	v_max_i32_e32 v0, 1, v0
	v_add_u32_e32 v11, v0, v10
	v_add_u32_e32 v0, 0x1ff, v7
	v_ashrrev_i32_e32 v0, 9, v0
	v_max_i32_e32 v0, 1, v0
	v_add_u32_e32 v12, v0, v11
	v_add_u32_e32 v0, 0x1ff, v8
	v_ashrrev_i32_e32 v0, 9, v0
	v_add_u32_e32 v5, v6, v4
	v_max_i32_e32 v0, 1, v0
	s_add_i32 s3, 0, 0x20060
	v_add_u32_e32 v6, v7, v5
	v_add_u32_e32 v13, v0, v12
	v_mov_b32_e32 v0, s3
	s_add_i32 s3, 0, 0x202e0
	v_add_u32_e32 v7, v8, v6
	ds_write_b128 v0, v[10:13]
	v_mov_b32_e32 v0, s3
	ds_write_b128 v0, v[4:7]
	v_add_u32_e32 v0, 0x1ff, v9
	v_ashrrev_i32_e32 v0, 9, v0
	v_max_i32_e32 v0, 1, v0
	v_add_u32_e32 v8, v0, v13
	s_waitcnt lgkmcnt(2)
	v_add_u32_e32 v0, 0x1ff, v14
	v_ashrrev_i32_e32 v0, 9, v0
	v_max_i32_e32 v0, 1, v0
	v_add_u32_e32 v4, v9, v7
	v_add_u32_e32 v9, v0, v8
	v_add_u32_e32 v0, 0x1ff, v15
	v_ashrrev_i32_e32 v0, 9, v0
	v_max_i32_e32 v0, 1, v0
	v_add_u32_e32 v10, v0, v9
	v_add_u32_e32 v0, 0x1ff, v16
	v_ashrrev_i32_e32 v0, 9, v0
	v_max_i32_e32 v0, 1, v0
	s_add_i32 s3, 0, 0x20070
	v_add_u32_e32 v5, v14, v4
	v_add_u32_e32 v11, v0, v10
	v_mov_b32_e32 v0, s3
	s_add_i32 s3, 0, 0x202f0
	v_add_u32_e32 v6, v15, v5
	ds_write_b128 v0, v[8:11]
	v_mov_b32_e32 v0, s3
	s_add_i32 s3, 0, 0x201c0
	v_add_u32_e32 v7, v16, v6
	v_mov_b32_e32 v1, s3
	ds_write_b128 v0, v[4:7]
	v_add_u32_e32 v4, v17, v7
	ds_read_b128 v[6:9], v1
	v_add_u32_e32 v0, 0x1ff, v17
	v_ashrrev_i32_e32 v0, 9, v0
	v_max_i32_e32 v0, 1, v0
	s_add_i32 s3, 0, 0x201d0
	v_add_u32_e32 v10, v0, v11
	v_mov_b32_e32 v0, s3
	ds_read_b128 v[14:17], v0
	s_waitcnt lgkmcnt(1)
	v_add_u32_e32 v0, 0x1ff, v6
	v_ashrrev_i32_e32 v0, 9, v0
	v_max_i32_e32 v0, 1, v0
	v_add_u32_e32 v11, v0, v10
	v_add_u32_e32 v0, 0x1ff, v7
	v_ashrrev_i32_e32 v0, 9, v0
	v_max_i32_e32 v0, 1, v0
	v_add_u32_e32 v12, v0, v11
	v_add_u32_e32 v0, 0x1ff, v8
	v_ashrrev_i32_e32 v0, 9, v0
	v_add_u32_e32 v5, v6, v4
	v_max_i32_e32 v0, 1, v0
	s_add_i32 s3, 0, 0x20080
	v_add_u32_e32 v6, v7, v5
	v_add_u32_e32 v13, v0, v12
	v_mov_b32_e32 v0, s3
	s_add_i32 s3, 0, 0x20300
	v_add_u32_e32 v7, v8, v6
	ds_write_b128 v0, v[10:13]
	v_mov_b32_e32 v0, s3
	ds_write_b128 v0, v[4:7]
	v_add_u32_e32 v0, 0x1ff, v9
	v_ashrrev_i32_e32 v0, 9, v0
	v_max_i32_e32 v0, 1, v0
	v_add_u32_e32 v8, v0, v13
	s_waitcnt lgkmcnt(2)
	v_add_u32_e32 v0, 0x1ff, v14
	v_ashrrev_i32_e32 v0, 9, v0
	v_max_i32_e32 v0, 1, v0
	v_add_u32_e32 v4, v9, v7
	v_add_u32_e32 v9, v0, v8
	v_add_u32_e32 v0, 0x1ff, v15
	v_ashrrev_i32_e32 v0, 9, v0
	v_max_i32_e32 v0, 1, v0
	v_add_u32_e32 v10, v0, v9
	v_add_u32_e32 v0, 0x1ff, v16
	v_ashrrev_i32_e32 v0, 9, v0
	v_max_i32_e32 v0, 1, v0
	s_add_i32 s3, 0, 0x20090
	v_add_u32_e32 v5, v14, v4
	v_add_u32_e32 v11, v0, v10
	v_mov_b32_e32 v0, s3
	s_add_i32 s3, 0, 0x20310
	v_add_u32_e32 v6, v15, v5
	ds_write_b128 v0, v[8:11]
	v_mov_b32_e32 v0, s3
	s_add_i32 s3, 0, 0x201e0
	v_add_u32_e32 v7, v16, v6
	v_mov_b32_e32 v1, s3
	ds_write_b128 v0, v[4:7]
	v_add_u32_e32 v4, v17, v7
	ds_read_b128 v[6:9], v1
	v_add_u32_e32 v0, 0x1ff, v17
	v_ashrrev_i32_e32 v0, 9, v0
	v_max_i32_e32 v0, 1, v0
	s_add_i32 s3, 0, 0x201f0
	v_add_u32_e32 v10, v0, v11
	v_mov_b32_e32 v0, s3
	ds_read_b128 v[14:17], v0
	s_waitcnt lgkmcnt(1)
	v_add_u32_e32 v0, 0x1ff, v6
	v_ashrrev_i32_e32 v0, 9, v0
	v_max_i32_e32 v0, 1, v0
	v_add_u32_e32 v11, v0, v10
	v_add_u32_e32 v0, 0x1ff, v7
	v_ashrrev_i32_e32 v0, 9, v0
	v_max_i32_e32 v0, 1, v0
	v_add_u32_e32 v12, v0, v11
	v_add_u32_e32 v0, 0x1ff, v8
	v_ashrrev_i32_e32 v0, 9, v0
	v_add_u32_e32 v5, v6, v4
	v_max_i32_e32 v0, 1, v0
	s_add_i32 s3, 0, 0x200a0
	v_add_u32_e32 v6, v7, v5
	v_add_u32_e32 v13, v0, v12
	v_mov_b32_e32 v0, s3
	s_add_i32 s3, 0, 0x20320
	v_add_u32_e32 v7, v8, v6
	ds_write_b128 v0, v[10:13]
	v_mov_b32_e32 v0, s3
	ds_write_b128 v0, v[4:7]
	v_add_u32_e32 v0, 0x1ff, v9
	v_ashrrev_i32_e32 v0, 9, v0
	v_max_i32_e32 v0, 1, v0
	v_add_u32_e32 v8, v0, v13
	s_waitcnt lgkmcnt(2)
	v_add_u32_e32 v0, 0x1ff, v14
	v_ashrrev_i32_e32 v0, 9, v0
	v_max_i32_e32 v0, 1, v0
	v_add_u32_e32 v4, v9, v7
	v_add_u32_e32 v9, v0, v8
	v_add_u32_e32 v0, 0x1ff, v15
	v_ashrrev_i32_e32 v0, 9, v0
	v_max_i32_e32 v0, 1, v0
	v_add_u32_e32 v10, v0, v9
	v_add_u32_e32 v0, 0x1ff, v16
	v_ashrrev_i32_e32 v0, 9, v0
	v_max_i32_e32 v0, 1, v0
	s_add_i32 s3, 0, 0x200b0
	v_add_u32_e32 v5, v14, v4
	v_add_u32_e32 v11, v0, v10
	v_mov_b32_e32 v0, s3
	s_add_i32 s3, 0, 0x20330
	v_add_u32_e32 v6, v15, v5
	ds_write_b128 v0, v[8:11]
	v_mov_b32_e32 v0, s3
	s_add_i32 s3, 0, 0x20200
	v_add_u32_e32 v7, v16, v6
	v_mov_b32_e32 v1, s3
	ds_write_b128 v0, v[4:7]
	v_add_u32_e32 v4, v17, v7
	ds_read_b128 v[6:9], v1
	v_add_u32_e32 v0, 0x1ff, v17
	v_ashrrev_i32_e32 v0, 9, v0
	v_max_i32_e32 v0, 1, v0
	s_add_i32 s3, 0, 0x20210
	v_add_u32_e32 v10, v0, v11
	v_mov_b32_e32 v0, s3
	ds_read_b128 v[14:17], v0
	s_waitcnt lgkmcnt(1)
	v_add_u32_e32 v0, 0x1ff, v6
	v_ashrrev_i32_e32 v0, 9, v0
	v_max_i32_e32 v0, 1, v0
	v_add_u32_e32 v11, v0, v10
	v_add_u32_e32 v0, 0x1ff, v7
	v_ashrrev_i32_e32 v0, 9, v0
	v_max_i32_e32 v0, 1, v0
	v_add_u32_e32 v12, v0, v11
	v_add_u32_e32 v0, 0x1ff, v8
	v_ashrrev_i32_e32 v0, 9, v0
	v_add_u32_e32 v5, v6, v4
	v_max_i32_e32 v0, 1, v0
	s_add_i32 s3, 0, 0x200c0
	v_add_u32_e32 v6, v7, v5
	v_add_u32_e32 v13, v0, v12
	v_mov_b32_e32 v0, s3
	s_add_i32 s3, 0, 0x20340
	v_add_u32_e32 v7, v8, v6
	ds_write_b128 v0, v[10:13]
	v_mov_b32_e32 v0, s3
	ds_write_b128 v0, v[4:7]
	v_add_u32_e32 v0, 0x1ff, v9
	v_ashrrev_i32_e32 v0, 9, v0
	v_max_i32_e32 v0, 1, v0
	v_add_u32_e32 v8, v0, v13
	s_waitcnt lgkmcnt(2)
	v_add_u32_e32 v0, 0x1ff, v14
	v_ashrrev_i32_e32 v0, 9, v0
	v_max_i32_e32 v0, 1, v0
	v_add_u32_e32 v4, v9, v7
	v_add_u32_e32 v9, v0, v8
	v_add_u32_e32 v0, 0x1ff, v15
	v_ashrrev_i32_e32 v0, 9, v0
	v_max_i32_e32 v0, 1, v0
	v_add_u32_e32 v10, v0, v9
	v_add_u32_e32 v0, 0x1ff, v16
	v_ashrrev_i32_e32 v0, 9, v0
	v_max_i32_e32 v0, 1, v0
	s_add_i32 s3, 0, 0x200d0
	v_add_u32_e32 v5, v14, v4
	v_add_u32_e32 v11, v0, v10
	v_mov_b32_e32 v0, s3
	s_add_i32 s3, 0, 0x20350
	v_add_u32_e32 v6, v15, v5
	ds_write_b128 v0, v[8:11]
	v_mov_b32_e32 v0, s3
	s_add_i32 s3, 0, 0x20220
	v_add_u32_e32 v7, v16, v6
	v_mov_b32_e32 v1, s3
	ds_write_b128 v0, v[4:7]
	v_add_u32_e32 v4, v17, v7
	ds_read_b128 v[6:9], v1
	v_add_u32_e32 v0, 0x1ff, v17
	v_ashrrev_i32_e32 v0, 9, v0
	v_max_i32_e32 v0, 1, v0
	s_add_i32 s3, 0, 0x20230
	v_add_u32_e32 v10, v0, v11
	v_mov_b32_e32 v0, s3
	ds_read_b128 v[14:17], v0
	s_waitcnt lgkmcnt(1)
	v_add_u32_e32 v0, 0x1ff, v6
	v_ashrrev_i32_e32 v0, 9, v0
	v_max_i32_e32 v0, 1, v0
	v_add_u32_e32 v11, v0, v10
	v_add_u32_e32 v0, 0x1ff, v7
	v_ashrrev_i32_e32 v0, 9, v0
	v_max_i32_e32 v0, 1, v0
	v_add_u32_e32 v12, v0, v11
	v_add_u32_e32 v0, 0x1ff, v8
	v_ashrrev_i32_e32 v0, 9, v0
	v_add_u32_e32 v5, v6, v4
	v_max_i32_e32 v0, 1, v0
	s_add_i32 s3, 0, 0x200e0
	v_add_u32_e32 v6, v7, v5
	v_add_u32_e32 v13, v0, v12
	v_mov_b32_e32 v0, s3
	s_add_i32 s3, 0, 0x20360
	v_add_u32_e32 v7, v8, v6
	ds_write_b128 v0, v[10:13]
	v_mov_b32_e32 v0, s3
	ds_write_b128 v0, v[4:7]
	v_add_u32_e32 v0, 0x1ff, v9
	v_ashrrev_i32_e32 v0, 9, v0
	v_max_i32_e32 v0, 1, v0
	v_add_u32_e32 v8, v0, v13
	s_waitcnt lgkmcnt(2)
	v_add_u32_e32 v0, 0x1ff, v14
	v_ashrrev_i32_e32 v0, 9, v0
	v_max_i32_e32 v0, 1, v0
	v_add_u32_e32 v4, v9, v7
	v_add_u32_e32 v9, v0, v8
	v_add_u32_e32 v0, 0x1ff, v15
	v_ashrrev_i32_e32 v0, 9, v0
	v_max_i32_e32 v0, 1, v0
	v_add_u32_e32 v10, v0, v9
	v_add_u32_e32 v0, 0x1ff, v16
	v_ashrrev_i32_e32 v0, 9, v0
	v_add_u32_e32 v5, v14, v4
	v_max_i32_e32 v0, 1, v0
	s_add_i32 s3, 0, 0x200f0
	v_add_u32_e32 v6, v15, v5
	v_add_u32_e32 v11, v0, v10
	v_mov_b32_e32 v0, s3
	s_add_i32 s3, 0, 0x20370
	v_add_u32_e32 v7, v16, v6
	ds_write_b128 v0, v[8:11]
	v_mov_b32_e32 v0, s3
	ds_write_b128 v0, v[4:7]
	v_add_u32_e32 v0, 0x1ff, v17
	v_ashrrev_i32_e32 v0, 9, v0
	v_max_i32_e32 v0, 1, v0
	s_add_i32 s3, 0, 0x20100
	v_add_u32_e32 v0, v0, v11
	v_mov_b32_e32 v1, s3
	ds_write_b32 v1, v0
